# wo output stores nt
# speedup vs baseline: 1.0508x; 1.0223x over previous
.LBB2_6:
	s_or_b64 exec, exec, s[0:1]
	s_movk_i32 s0, 0x100
	v_cmp_gt_u32_e32 vcc, s0, v0
	s_waitcnt lgkmcnt(0)
	s_barrier
	s_and_saveexec_b64 s[0:1], vcc
	s_cbranch_execz .LBB2_8
	v_add3_u32 v68, 0, v66, v67
	s_waitcnt vmcnt(6)
	ds_read2st64_b32 v[70:71], v68 offset1:1
	v_and_b32_e32 v0, 64, v0
	v_lshlrev_b32_e32 v69, 2, v103
	v_or3_b32 v0, v0, s2, v1
	s_waitcnt vmcnt(2)
	v_or3_b32 v78, v106, v69, s3
	v_ashrrev_i32_e32 v1, 31, v0
	v_lshl_add_u64 v[0:1], v[0:1], 2, s[8:9]
	s_waitcnt lgkmcnt(0)
	v_add_f32_e32 v50, v50, v70
	v_lshlrev_b32_e32 v66, 13, v78
	v_mov_b32_e32 v67, 0
	v_mul_f32_e32 v50, 0x3a800000, v50
	v_lshl_add_u64 v[78:79], v[0:1], 0, v[66:67]
	ds_read2st64_b32 v[72:73], v68 offset0:2 offset1:3
	ds_read2st64_b32 v[74:75], v68 offset0:4 offset1:5
	ds_read2st64_b32 v[76:77], v68 offset0:6 offset1:7
	global_store_dword v[78:79], v50, off nt
	v_add_f32_e32 v50, v51, v71
	v_mul_f32_e32 v80, 0x3a800000, v50
	v_or_b32_e32 v50, 0x2000, v66
	v_mov_b32_e32 v51, v67
	v_lshl_add_u64 v[70:71], v[0:1], 0, v[50:51]
	global_store_dword v[70:71], v80, off nt
	s_waitcnt lgkmcnt(2)
	v_add_f32_e32 v52, v52, v72
	v_or_b32_e32 v70, 0x4000, v66
	v_mov_b32_e32 v71, v67
	v_mul_f32_e32 v52, 0x3a800000, v52
	v_lshl_add_u64 v[80:81], v[0:1], 0, v[70:71]
	global_store_dword v[80:81], v52, off nt
	v_add_f32_e32 v52, v53, v73
	v_mul_f32_e32 v80, 0x3a800000, v52
	v_or_b32_e32 v52, 0x6000, v66
	v_mov_b32_e32 v53, v67
	v_lshl_add_u64 v[72:73], v[0:1], 0, v[52:53]
	global_store_dword v[72:73], v80, off nt
	s_waitcnt lgkmcnt(1)
	v_add_f32_e32 v54, v54, v74
	v_or_b32_e32 v72, 0x10000, v66
	v_mov_b32_e32 v73, v67
	v_mul_f32_e32 v54, 0x3a800000, v54
	v_lshl_add_u64 v[72:73], v[0:1], 0, v[72:73]
	global_store_dword v[72:73], v54, off nt
	v_add_f32_e32 v54, v55, v75
	v_mul_f32_e32 v74, 0x3a800000, v54
	v_or_b32_e32 v54, 0x12000, v66
	v_mov_b32_e32 v55, v67
	v_lshl_add_u64 v[54:55], v[0:1], 0, v[54:55]
	global_store_dword v[54:55], v74, off nt
	s_waitcnt lgkmcnt(0)
	v_add_f32_e32 v56, v56, v76
	v_or_b32_e32 v74, 0x14000, v66
	v_mov_b32_e32 v75, v67
	v_mul_f32_e32 v56, 0x3a800000, v56
	v_lshl_add_u64 v[74:75], v[0:1], 0, v[74:75]
	global_store_dword v[74:75], v56, off nt
	v_add_f32_e32 v56, v57, v77
	ds_read2st64_b32 v[76:77], v68 offset0:8 offset1:9
	v_mul_f32_e32 v80, 0x3a800000, v56
	v_or_b32_e32 v56, 0x16000, v66
	v_mov_b32_e32 v57, v67
	v_lshl_add_u64 v[56:57], v[0:1], 0, v[56:57]
	s_waitcnt lgkmcnt(0)
	v_add_f32_e32 v58, v58, v76
	s_waitcnt vmcnt(8)
	v_or_b32_e32 v86, 0x20000, v66
	v_mov_b32_e32 v87, v67
	global_store_dword v[56:57], v80, off nt
	v_mul_f32_e32 v58, 0x3a800000, v58
	v_lshl_add_u64 v[86:87], v[0:1], 0, v[86:87]
	ds_read2st64_b32 v[80:81], v68 offset0:10 offset1:11
	ds_read2st64_b32 v[82:83], v68 offset0:12 offset1:13
	ds_read2st64_b32 v[84:85], v68 offset0:14 offset1:15
	global_store_dword v[86:87], v58, off nt
	v_add_f32_e32 v58, v59, v77
	v_mul_f32_e32 v76, 0x3a800000, v58
	v_or_b32_e32 v58, 0x22000, v66
	v_mov_b32_e32 v59, v67
	v_lshl_add_u64 v[58:59], v[0:1], 0, v[58:59]
	global_store_dword v[58:59], v76, off nt
	s_waitcnt lgkmcnt(2)
	v_add_f32_e32 v60, v60, v80
	v_or_b32_e32 v76, 0x24000, v66
	v_mov_b32_e32 v77, v67
	v_mul_f32_e32 v60, 0x3a800000, v60
	v_lshl_add_u64 v[76:77], v[0:1], 0, v[76:77]
	global_store_dword v[76:77], v60, off nt
	v_add_f32_e32 v60, v61, v81
	v_mul_f32_e32 v80, 0x3a800000, v60
	v_or_b32_e32 v60, 0x26000, v66
	v_mov_b32_e32 v61, v67
	v_lshl_add_u64 v[60:61], v[0:1], 0, v[60:61]
	global_store_dword v[60:61], v80, off nt
	s_waitcnt lgkmcnt(1)
	v_add_f32_e32 v62, v62, v82
	v_or_b32_e32 v80, 0x30000, v66
	v_mov_b32_e32 v81, v67
	v_mul_f32_e32 v62, 0x3a800000, v62
	v_lshl_add_u64 v[80:81], v[0:1], 0, v[80:81]
	global_store_dword v[80:81], v62, off nt
	v_add_f32_e32 v62, v63, v83
	v_mul_f32_e32 v82, 0x3a800000, v62
	v_or_b32_e32 v62, 0x32000, v66
	v_mov_b32_e32 v63, v67
	v_lshl_add_u64 v[62:63], v[0:1], 0, v[62:63]
	global_store_dword v[62:63], v82, off nt
	s_waitcnt lgkmcnt(0)
	v_add_f32_e32 v64, v64, v84
	v_or_b32_e32 v82, 0x34000, v66
	v_mov_b32_e32 v83, v67
	v_mul_f32_e32 v64, 0x3a800000, v64
	v_lshl_add_u64 v[82:83], v[0:1], 0, v[82:83]
	global_store_dword v[82:83], v64, off nt
	v_add_f32_e32 v64, v65, v85
	v_or_b32_e32 v66, 0x36000, v66
	v_mul_f32_e32 v84, 0x3a800000, v64
	v_lshl_add_u64 v[64:65], v[0:1], 0, v[66:67]
	global_store_dword v[64:65], v84, off nt
	ds_read2st64_b32 v[84:85], v68 offset0:16 offset1:17
	s_mov_b64 s[0:1], 0x80
	ds_read2st64_b32 v[90:91], v68 offset0:18 offset1:19
	ds_read2st64_b32 v[92:93], v68 offset0:20 offset1:21
	s_waitcnt vmcnt(16)
	ds_read2st64_b32 v[94:95], v68 offset0:22 offset1:23
	v_lshl_add_u64 v[88:89], v[0:1], 0, s[0:1]
	s_waitcnt lgkmcnt(3)
	v_add_f32_e32 v34, v34, v84
	v_mul_f32_e32 v34, 0x3a800000, v34
	global_store_dword v[78:79], v34, off offset:128 nt
	v_add_f32_e32 v34, v35, v85
	v_mul_f32_e32 v66, 0x3a800000, v34
	v_lshl_add_u64 v[34:35], v[88:89], 0, v[50:51]
	global_store_dword v[34:35], v66, off nt
	s_waitcnt lgkmcnt(2)
	v_add_f32_e32 v34, v36, v90
	v_mul_f32_e32 v36, 0x3a800000, v34
	v_lshl_add_u64 v[34:35], v[88:89], 0, v[70:71]
	global_store_dword v[34:35], v36, off nt
	v_add_f32_e32 v34, v37, v91
	v_mul_f32_e32 v36, 0x3a800000, v34
	v_lshl_add_u64 v[34:35], v[88:89], 0, v[52:53]
	global_store_dword v[34:35], v36, off nt
	s_waitcnt lgkmcnt(1)
	v_add_f32_e32 v34, v38, v92
	v_mul_f32_e32 v34, 0x3a800000, v34
	global_store_dword v[72:73], v34, off offset:128 nt
	v_add_f32_e32 v34, v39, v93
	v_mul_f32_e32 v34, 0x3a800000, v34
	global_store_dword v[54:55], v34, off offset:128 nt
	s_waitcnt lgkmcnt(0)
	v_add_f32_e32 v34, v40, v94
	v_mul_f32_e32 v34, 0x3a800000, v34
	global_store_dword v[74:75], v34, off offset:128 nt
	v_add_f32_e32 v34, v41, v95
	v_mul_f32_e32 v36, 0x3a800000, v34
	ds_read2st64_b32 v[34:35], v68 offset0:24 offset1:25
	global_store_dword v[56:57], v36, off offset:128 nt
	ds_read2st64_b32 v[36:37], v68 offset0:26 offset1:27
	ds_read2st64_b32 v[38:39], v68 offset0:28 offset1:29
	ds_read2st64_b32 v[40:41], v68 offset0:30 offset1:31
	s_waitcnt lgkmcnt(3)
	v_add_f32_e32 v34, v42, v34
	v_mul_f32_e32 v34, 0x3a800000, v34
	global_store_dword v[86:87], v34, off offset:128 nt
	v_add_f32_e32 v34, v43, v35
	v_mul_f32_e32 v34, 0x3a800000, v34
	global_store_dword v[58:59], v34, off offset:128 nt
	s_waitcnt lgkmcnt(2)
	v_add_f32_e32 v34, v44, v36
	v_mul_f32_e32 v34, 0x3a800000, v34
	global_store_dword v[76:77], v34, off offset:128 nt
	v_add_f32_e32 v34, v45, v37
	v_mul_f32_e32 v34, 0x3a800000, v34
	global_store_dword v[60:61], v34, off offset:128 nt
	s_waitcnt lgkmcnt(1)
	v_add_f32_e32 v34, v46, v38
	v_mul_f32_e32 v34, 0x3a800000, v34
	global_store_dword v[80:81], v34, off offset:128 nt
	v_add_f32_e32 v34, v47, v39
	v_mul_f32_e32 v34, 0x3a800000, v34
	global_store_dword v[62:63], v34, off offset:128 nt
	s_waitcnt lgkmcnt(0)
	v_add_f32_e32 v34, v48, v40
	v_mul_f32_e32 v34, 0x3a800000, v34
	global_store_dword v[82:83], v34, off offset:128 nt
	v_add_f32_e32 v34, v49, v41
	v_mul_f32_e32 v34, 0x3a800000, v34
	global_store_dword v[64:65], v34, off offset:128 nt
	ds_read2st64_b32 v[34:35], v68 offset0:32 offset1:33
	v_or3_b32 v42, v102, v69, s3
	v_lshlrev_b32_e32 v52, 13, v42
	ds_read2st64_b32 v[36:37], v68 offset0:34 offset1:35
	ds_read2st64_b32 v[38:39], v68 offset0:36 offset1:37
	ds_read2st64_b32 v[40:41], v68 offset0:38 offset1:39
	v_or_b32_e32 v66, 0x40000, v52
	s_waitcnt lgkmcnt(3)
	v_add_f32_e32 v18, v18, v34
	v_mul_f32_e32 v18, 0x3a800000, v18
	v_lshl_add_u64 v[42:43], v[0:1], 0, v[66:67]
	global_store_dword v[42:43], v18, off nt
	v_add_f32_e32 v18, v19, v35
	v_or_b32_e32 v66, 0x42000, v52
	v_mul_f32_e32 v34, 0x3a800000, v18
	v_lshl_add_u64 v[18:19], v[0:1], 0, v[66:67]
	s_waitcnt lgkmcnt(2)
	v_add_f32_e32 v20, v20, v36
	v_or_b32_e32 v66, 0x44000, v52
	global_store_dword v[18:19], v34, off nt
	v_mul_f32_e32 v20, 0x3a800000, v20
	v_lshl_add_u64 v[34:35], v[0:1], 0, v[66:67]
	global_store_dword v[34:35], v20, off nt
	v_add_f32_e32 v20, v21, v37
	v_or_b32_e32 v66, 0x46000, v52
	v_mul_f32_e32 v36, 0x3a800000, v20
	v_lshl_add_u64 v[20:21], v[0:1], 0, v[66:67]
	s_waitcnt lgkmcnt(1)
	v_add_f32_e32 v22, v22, v38
	v_or_b32_e32 v66, 0x50000, v52
	global_store_dword v[20:21], v36, off nt
	v_mul_f32_e32 v22, 0x3a800000, v22
	v_lshl_add_u64 v[36:37], v[0:1], 0, v[66:67]
	global_store_dword v[36:37], v22, off nt
	v_add_f32_e32 v22, v23, v39
	v_or_b32_e32 v66, 0x52000, v52
	v_mul_f32_e32 v38, 0x3a800000, v22
	v_lshl_add_u64 v[22:23], v[0:1], 0, v[66:67]
	s_waitcnt lgkmcnt(0)
	v_add_f32_e32 v24, v24, v40
	v_or_b32_e32 v66, 0x54000, v52
	global_store_dword v[22:23], v38, off nt
	v_mul_f32_e32 v24, 0x3a800000, v24
	v_lshl_add_u64 v[38:39], v[0:1], 0, v[66:67]
	global_store_dword v[38:39], v24, off nt
	v_add_f32_e32 v24, v25, v41
	ds_read2st64_b32 v[40:41], v68 offset0:40 offset1:41
	v_or_b32_e32 v66, 0x56000, v52
	v_mul_f32_e32 v44, 0x3a800000, v24
	v_lshl_add_u64 v[24:25], v[0:1], 0, v[66:67]
	global_store_dword v[24:25], v44, off nt
	ds_read2st64_b32 v[44:45], v68 offset0:42 offset1:43
	ds_read2st64_b32 v[46:47], v68 offset0:44 offset1:45
	ds_read2st64_b32 v[48:49], v68 offset0:46 offset1:47
	s_waitcnt lgkmcnt(3)
	v_add_f32_e32 v26, v26, v40
	v_or_b32_e32 v66, 0x60000, v52
	v_mul_f32_e32 v26, 0x3a800000, v26
	v_lshl_add_u64 v[50:51], v[0:1], 0, v[66:67]
	global_store_dword v[50:51], v26, off nt
	v_add_f32_e32 v26, v27, v41
	v_or_b32_e32 v66, 0x62000, v52
	v_mul_f32_e32 v40, 0x3a800000, v26
	v_lshl_add_u64 v[26:27], v[0:1], 0, v[66:67]
	s_waitcnt lgkmcnt(2)
	v_add_f32_e32 v28, v28, v44
	v_or_b32_e32 v66, 0x64000, v52
	global_store_dword v[26:27], v40, off nt
	v_mul_f32_e32 v28, 0x3a800000, v28
	v_lshl_add_u64 v[40:41], v[0:1], 0, v[66:67]
	global_store_dword v[40:41], v28, off nt
	v_add_f32_e32 v28, v29, v45
	v_or_b32_e32 v66, 0x66000, v52
	v_mul_f32_e32 v44, 0x3a800000, v28
	v_lshl_add_u64 v[28:29], v[0:1], 0, v[66:67]
	s_waitcnt lgkmcnt(1)
	v_add_f32_e32 v30, v30, v46
	v_or_b32_e32 v66, 0x70000, v52
	global_store_dword v[28:29], v44, off nt
	v_mul_f32_e32 v30, 0x3a800000, v30
	v_lshl_add_u64 v[44:45], v[0:1], 0, v[66:67]
	global_store_dword v[44:45], v30, off nt
	v_add_f32_e32 v30, v31, v47
	v_or_b32_e32 v66, 0x72000, v52
	v_mul_f32_e32 v46, 0x3a800000, v30
	v_lshl_add_u64 v[30:31], v[0:1], 0, v[66:67]
	s_waitcnt lgkmcnt(0)
	v_add_f32_e32 v32, v32, v48
	v_or_b32_e32 v66, 0x74000, v52
	global_store_dword v[30:31], v46, off nt
	v_mul_f32_e32 v32, 0x3a800000, v32
	v_lshl_add_u64 v[46:47], v[0:1], 0, v[66:67]
	global_store_dword v[46:47], v32, off nt
	v_add_f32_e32 v32, v33, v49
	v_mul_f32_e32 v48, 0x3a800000, v32
	ds_read2st64_b32 v[32:33], v68 offset0:48 offset1:49
	v_or_b32_e32 v66, 0x76000, v52
	v_lshl_add_u64 v[0:1], v[0:1], 0, v[66:67]
	global_store_dword v[0:1], v48, off nt
	ds_read2st64_b32 v[48:49], v68 offset0:50 offset1:51
	ds_read2st64_b32 v[52:53], v68 offset0:52 offset1:53
	ds_read2st64_b32 v[54:55], v68 offset0:54 offset1:55
	s_waitcnt lgkmcnt(3)
	v_add_f32_e32 v2, v2, v32
	v_mul_f32_e32 v2, 0x3a800000, v2
	global_store_dword v[42:43], v2, off offset:128 nt
	v_add_f32_e32 v2, v3, v33
	v_mul_f32_e32 v2, 0x3a800000, v2
	global_store_dword v[18:19], v2, off offset:128 nt
	s_waitcnt lgkmcnt(2)
	v_add_f32_e32 v2, v4, v48
	v_mul_f32_e32 v2, 0x3a800000, v2
	global_store_dword v[34:35], v2, off offset:128 nt
	v_add_f32_e32 v2, v5, v49
	v_mul_f32_e32 v2, 0x3a800000, v2
	global_store_dword v[20:21], v2, off offset:128 nt
	s_waitcnt lgkmcnt(1)
	v_add_f32_e32 v2, v6, v52
	v_mul_f32_e32 v2, 0x3a800000, v2
	global_store_dword v[36:37], v2, off offset:128 nt
	v_add_f32_e32 v2, v7, v53
	v_mul_f32_e32 v2, 0x3a800000, v2
	global_store_dword v[22:23], v2, off offset:128 nt
	s_waitcnt lgkmcnt(0)
	v_add_f32_e32 v2, v8, v54
	v_mul_f32_e32 v2, 0x3a800000, v2
	global_store_dword v[38:39], v2, off offset:128 nt
	v_add_f32_e32 v2, v9, v55
	v_mul_f32_e32 v4, 0x3a800000, v2
	ds_read2st64_b32 v[2:3], v68 offset0:56 offset1:57
	global_store_dword v[24:25], v4, off offset:128 nt
	ds_read2st64_b32 v[4:5], v68 offset0:58 offset1:59
	ds_read2st64_b32 v[6:7], v68 offset0:60 offset1:61
	ds_read2st64_b32 v[8:9], v68 offset0:62 offset1:63
	s_waitcnt lgkmcnt(3)
	v_add_f32_e32 v2, v10, v2
	v_mul_f32_e32 v2, 0x3a800000, v2
	global_store_dword v[50:51], v2, off offset:128 nt
	v_add_f32_e32 v2, v11, v3
	v_mul_f32_e32 v2, 0x3a800000, v2
	global_store_dword v[26:27], v2, off offset:128 nt
	s_waitcnt lgkmcnt(2)
	v_add_f32_e32 v2, v12, v4
	v_mul_f32_e32 v2, 0x3a800000, v2
	global_store_dword v[40:41], v2, off offset:128 nt
	v_add_f32_e32 v2, v13, v5
	v_mul_f32_e32 v2, 0x3a800000, v2
	global_store_dword v[28:29], v2, off offset:128 nt
	s_waitcnt lgkmcnt(1)
	v_add_f32_e32 v2, v14, v6
	v_mul_f32_e32 v2, 0x3a800000, v2
	global_store_dword v[44:45], v2, off offset:128 nt
	v_add_f32_e32 v2, v15, v7
	v_mul_f32_e32 v2, 0x3a800000, v2
	global_store_dword v[30:31], v2, off offset:128 nt
	s_waitcnt lgkmcnt(0)
	v_add_f32_e32 v2, v16, v8
	v_mul_f32_e32 v2, 0x3a800000, v2
	global_store_dword v[46:47], v2, off offset:128 nt
	v_add_f32_e32 v2, v17, v9
	v_mul_f32_e32 v2, 0x3a800000, v2
	global_store_dword v[0:1], v2, off offset:128 nt
